# code placement: padded so every fp8 GEMM loop sits at the baseline's byte phase (MoE loops were shifted 4 mod 8)
# baseline (speedup 1.0000x reference)
; __device__ __forceinline__ unsigned xb_ld(unsigned* p)              { return __hip_atomic_load(p, __ATOMIC_RELAXED, __HIP_MEMORY_SCOPE_AGENT); }
; __device__ __forceinline__ void xcd_barrier_complete(unsigned* bar, unsigned x, unsigned& nloc, unsigned& nx) {
;     const unsigned G = gridDim.x * gridDim.y * gridDim.z;
;     unsigned sum, cnt, mine, sp = 0u;
;     for (;;) {
;         sum = 0u; cnt = 0u; mine = 0u;
; #pragma unroll
;         for (unsigned j = 0; j < 16; ++j) { const unsigned c = xb_ld(&bar[XB_XCNT(j)]); sum += c; cnt += (c > 0u) ? 1u : 0u; mine = (j == x) ? c : mine; }
; __device__ __forceinline__ void xcd_barrier(const XcdBarrier& b) {
;     asm volatile("s_waitcnt vmcnt(0)" ::: "memory");
;     __syncthreads();
;     if (threadIdx.x == 0) {
;         unsigned* bar = b.bar;
;         __builtin_amdgcn_s_waitcnt(0);
;         unsigned nloc = b.st[0], nx = b.st[1];
;         if (nloc == 0u) { xcd_barrier_complete(bar, b.x, nloc, nx); b.st[0] = nloc; b.st[1] = nx; }
.Lsw_done:
	s_nop 0
	s_nop 0
	s_nop 0
	s_nop 0
	s_nop 0
	s_nop 0
	s_nop 0
	s_nop 0
	s_nop 0
	s_nop 0
	v_readlane_b32 s2, v253, 0
	v_readlane_b32 s3, v253, 1
	s_getreg_b32 s4, hwreg(HW_REG_XCC_ID, 0, 4)
	s_waitcnt vmcnt(0)
	s_barrier
	s_mov_b64 s[0:1], exec
	v_readlane_b32 s6, v253, 5
	v_readlane_b32 s7, v253, 6
	s_and_b64 s[6:7], s[0:1], s[6:7]
	v_readlane_b32 s76, v255, 19
	v_readlane_b32 s78, v255, 21
	v_readlane_b32 s77, v255, 20
	s_mov_b64 exec, s[6:7]
	s_cbranch_execz .LBB0_413
	v_readlane_b32 s5, v254, 47
	s_load_dwordx2 s[2:3], s[2:3], 0xa0
	s_waitcnt vmcnt(0) expcnt(0) lgkmcnt(0)
	v_mov_b32_e32 v0, s5
	ds_read_b32 v2, v0
	v_readlane_b32 s5, v254, 48
	s_and_b32 s50, s4, 15
	s_waitcnt lgkmcnt(0)
	v_cmp_ne_u32_e32 vcc, 0, v2
	v_mov_b32_e32 v0, s5
	ds_read_b32 v0, v0
	s_cbranch_vccnz .LBB0_377
	v_readlane_b32 s4, v253, 2
	v_readlane_b32 s5, v253, 3
	s_load_dwordx2 s[8:9], s[4:5], 0x4
	s_add_u32 s4, s2, 0x4200
	s_addc_u32 s5, s3, 0
	s_add_u32 s6, s2, 0x4400
	s_addc_u32 s7, s3, 0
	s_waitcnt lgkmcnt(0)
	s_mul_i32 s51, s8, s74
	s_add_u32 s8, s2, 0x4500
	s_mul_i32 s51, s51, s9
	s_addc_u32 s9, s3, 0
	s_add_u32 s10, s2, 0x4600
	s_addc_u32 s11, s3, 0
	s_add_u32 s12, s2, 0x4700
	s_addc_u32 s13, s3, 0
	s_add_u32 s14, s2, 0x4800
	s_addc_u32 s15, s3, 0
	s_add_u32 s16, s2, 0x4900
	s_addc_u32 s17, s3, 0
	s_add_u32 s18, s2, 0x4a00
	s_addc_u32 s19, s3, 0
	s_add_u32 s20, s2, 0x4b00
	s_addc_u32 s21, s3, 0
	s_add_u32 s22, s2, 0x4c00
	s_addc_u32 s23, s3, 0
	s_add_u32 s24, s2, 0x4d00
	s_addc_u32 s25, s3, 0
	s_add_u32 s26, s2, 0x4e00
	s_addc_u32 s27, s3, 0
	s_add_u32 s28, s2, 0x4f00
	s_addc_u32 s29, s3, 0
	s_add_u32 s30, s2, 0x5000
	s_addc_u32 s31, s3, 0
	s_add_u32 s34, s2, 0x5100
	s_addc_u32 s35, s3, 0
	s_add_u32 s36, s2, 0x5200
	s_addc_u32 s37, s3, 0
	s_add_u32 s40, s2, 0x5300
	s_addc_u32 s41, s3, 0
	s_mov_b32 s52, 1
	s_branch .LBB0_365

; #define LAS __attribute__((address_space(3)))
; #define FRESH_TID() do { ap = fresh_args(); ws = ap->ws; unsigned m1_ = ~0u; asm volatile("" : "+s"(m1_)); lane = (int)__builtin_amdgcn_mbcnt_hi(m1_, __builtin_amdgcn_mbcnt_lo(m1_, 0u)); asm volatile("" : "+v"(lane)); wave = wave0; tid = wave0 * 64 + lane; } while (0)
; __device__ __forceinline__ void moe_table_build(LAS unsigned char* lds, const unsigned* cnt, int tid) {
;     if (tid < NE) { const int n = (int)__hip_atomic_load(cnt + 64 * tid, RLX_AGENT); ((LAS int*)(lds + MOE_TAB_OFF))[16 + tid] = n; }
; template <unsigned MASK, bool ONE>
; __global__ void __launch_bounds__(NTHREADS, 2) fwd_kernel(Args a_unused) {
;     ...
;         if (IN(P + 9, 10)) { FRESH_TID();
;             pg8::moe_table_build(lds, cntl, tid);
.LBB0_925:
	s_or_b64 exec, exec, s[0:1]
	s_nop 0
	s_nop 0
	s_nop 0
	s_nop 0
	s_nop 0
	s_nop 0
	s_nop 0
	v_readlane_b32 s101, v255, 17
	s_movk_i32 s100, 0x100
	s_cmp_eq_u32 s101, 0
	s_cselect_b32 s100, 0xa0, s100
	s_cselect_b32 s101, 96, 0
	v_readlane_b32 s0, v253, 0
	v_readlane_b32 s1, v253, 1
	s_waitcnt lgkmcnt(0)
	s_barrier
	s_load_dwordx2 s[6:7], s[0:1], 0xa0
	s_mov_b32 s0, s38
	s_nop 0
	v_mbcnt_lo_u32_b32 v0, s0, 0
	v_mbcnt_hi_u32_b32 v0, s0, v0
	s_nop 0
	v_add_u32_e32 v1, s78, v0
	v_cmp_gt_i32_e32 vcc, 16, v1
	s_and_saveexec_b64 s[0:1], vcc
	s_cbranch_execz .LBB0_927
	s_lshl_b64 s[2:3], s[96:97], 2
	s_waitcnt lgkmcnt(0)
	s_add_u32 s2, s6, s2
	v_lshlrev_b32_e32 v2, 6, v1
	s_addc_u32 s3, s7, s3
	v_ashrrev_i32_e32 v3, 31, v2
	v_lshl_add_u64 v[2:3], v[2:3], 2, s[2:3]
	v_add_co_u32_e32 v2, vcc, 0x10000, v2
	v_readlane_b32 s2, v255, 23
	s_nop 0
	v_addc_co_u32_e32 v3, vcc, 0, v3, vcc
	global_load_dword v2, v[2:3], off sc1
	v_lshl_add_u32 v3, v1, 2, s2
	s_waitcnt vmcnt(0)
	ds_write_b32 v3, v2 offset:64
